# speedup vs baseline: 1.0400x; 1.0051x over previous
.Lpro_noflag:
	s_or_b64 exec, exec, s[38:39]
	v_lshlrev_b32_e32 v41, 2, v204
	v_and_b32_e32 v41, 28, v41
	global_load_dword v38, v41, s[10:11] sc1
	v_lshrrev_b32_e32 v202, 4, v204
	v_and_b32_e32 v31, 15, v204
	v_xor_b32_e32 v32, v31, v202
	v_xor_b32_e32 v33, 4, v32
	v_lshlrev_b32_e32 v34, 8, v202
	v_or_b32_e32 v35, 0x10000, v40
	v_add_u32_e32 v34, v34, v35
	v_lshl_add_u32 v24, v32, 4, v34
	v_lshl_add_u32 v25, v33, 4, v34
	v_pk_mul_f32 v[106:107], v[106:107], s[44:45] op_sel_hi:[1,0]
	v_pk_mul_f32 v[108:109], v[108:109], s[44:45] op_sel_hi:[1,0]
	v_pk_mul_f32 v[110:111], v[110:111], s[44:45] op_sel_hi:[1,0]
	v_pk_mul_f32 v[112:113], v[112:113], s[44:45] op_sel_hi:[1,0]
	v_cvt_pk_bf16_f32 v12, v106, v107
	v_cvt_pk_bf16_f32 v13, v108, v109
	v_cvt_pk_bf16_f32 v14, v110, v111
	v_cvt_pk_bf16_f32 v15, v112, v113
	ds_write_b128 v24, v[12:15] offset:0
	v_pk_mul_f32 v[114:115], v[114:115], s[44:45] op_sel_hi:[1,0]
	v_pk_mul_f32 v[116:117], v[116:117], s[44:45] op_sel_hi:[1,0]
	v_pk_mul_f32 v[118:119], v[118:119], s[44:45] op_sel_hi:[1,0]
	v_pk_mul_f32 v[120:121], v[120:121], s[44:45] op_sel_hi:[1,0]
	v_cvt_pk_bf16_f32 v16, v114, v115
	v_cvt_pk_bf16_f32 v17, v116, v117
	v_cvt_pk_bf16_f32 v18, v118, v119
	v_cvt_pk_bf16_f32 v19, v120, v121
	ds_write_b128 v25, v[16:19] offset:1024
	v_pk_mul_f32 v[122:123], v[122:123], s[44:45] op_sel_hi:[1,0]
	v_pk_mul_f32 v[124:125], v[124:125], s[44:45] op_sel_hi:[1,0]
	v_pk_mul_f32 v[126:127], v[126:127], s[44:45] op_sel_hi:[1,0]
	v_pk_mul_f32 v[128:129], v[128:129], s[44:45] op_sel_hi:[1,0]
	v_cvt_pk_bf16_f32 v20, v122, v123
	v_cvt_pk_bf16_f32 v21, v124, v125
	v_cvt_pk_bf16_f32 v22, v126, v127
	v_cvt_pk_bf16_f32 v23, v128, v129
	ds_write_b128 v24, v[20:23] offset:2048
	v_pk_mul_f32 v[130:131], v[130:131], s[44:45] op_sel_hi:[1,0]
	v_pk_mul_f32 v[132:133], v[132:133], s[44:45] op_sel_hi:[1,0]
	v_pk_mul_f32 v[134:135], v[134:135], s[44:45] op_sel_hi:[1,0]
	v_pk_mul_f32 v[136:137], v[136:137], s[44:45] op_sel_hi:[1,0]
	v_cvt_pk_bf16_f32 v12, v130, v131
	v_cvt_pk_bf16_f32 v13, v132, v133
	v_cvt_pk_bf16_f32 v14, v134, v135
	v_cvt_pk_bf16_f32 v15, v136, v137
	ds_write_b128 v25, v[12:15] offset:3072
	v_pk_mul_f32 v[138:139], v[138:139], s[44:45] op_sel_hi:[1,0]
	v_pk_mul_f32 v[140:141], v[140:141], s[44:45] op_sel_hi:[1,0]
	v_pk_mul_f32 v[142:143], v[142:143], s[44:45] op_sel_hi:[1,0]
	v_pk_mul_f32 v[144:145], v[144:145], s[44:45] op_sel_hi:[1,0]
	v_cvt_pk_bf16_f32 v16, v138, v139
	v_cvt_pk_bf16_f32 v17, v140, v141
	v_cvt_pk_bf16_f32 v18, v142, v143
	v_cvt_pk_bf16_f32 v19, v144, v145
	ds_write_b128 v24, v[16:19] offset:4096
	v_pk_mul_f32 v[146:147], v[146:147], s[44:45] op_sel_hi:[1,0]
	v_pk_mul_f32 v[148:149], v[148:149], s[44:45] op_sel_hi:[1,0]
	v_pk_mul_f32 v[150:151], v[150:151], s[44:45] op_sel_hi:[1,0]
	v_pk_mul_f32 v[152:153], v[152:153], s[44:45] op_sel_hi:[1,0]
	v_cvt_pk_bf16_f32 v20, v146, v147
	v_cvt_pk_bf16_f32 v21, v148, v149
	v_cvt_pk_bf16_f32 v22, v150, v151
	v_cvt_pk_bf16_f32 v23, v152, v153
	ds_write_b128 v25, v[20:23] offset:5120
	v_pk_mul_f32 v[154:155], v[154:155], s[44:45] op_sel_hi:[1,0]
	v_pk_mul_f32 v[156:157], v[156:157], s[44:45] op_sel_hi:[1,0]
	v_pk_mul_f32 v[158:159], v[158:159], s[44:45] op_sel_hi:[1,0]
	v_pk_mul_f32 v[160:161], v[160:161], s[44:45] op_sel_hi:[1,0]
	v_cvt_pk_bf16_f32 v12, v154, v155
	v_cvt_pk_bf16_f32 v13, v156, v157
	v_cvt_pk_bf16_f32 v14, v158, v159
	v_cvt_pk_bf16_f32 v15, v160, v161
	ds_write_b128 v24, v[12:15] offset:6144
	v_pk_mul_f32 v[162:163], v[162:163], s[44:45] op_sel_hi:[1,0]
	v_pk_mul_f32 v[164:165], v[164:165], s[44:45] op_sel_hi:[1,0]
	v_pk_mul_f32 v[166:167], v[166:167], s[44:45] op_sel_hi:[1,0]
	v_pk_mul_f32 v[168:169], v[168:169], s[44:45] op_sel_hi:[1,0]
	v_cvt_pk_bf16_f32 v16, v162, v163
	v_cvt_pk_bf16_f32 v17, v164, v165
	v_cvt_pk_bf16_f32 v18, v166, v167
	v_cvt_pk_bf16_f32 v19, v168, v169
	ds_write_b128 v25, v[16:19] offset:7168
	v_pk_mul_f32 v[170:171], v[170:171], s[44:45] op_sel_hi:[1,0]
	v_pk_mul_f32 v[172:173], v[172:173], s[44:45] op_sel_hi:[1,0]
	v_pk_mul_f32 v[174:175], v[174:175], s[44:45] op_sel_hi:[1,0]
	v_pk_mul_f32 v[176:177], v[176:177], s[44:45] op_sel_hi:[1,0]
	v_cvt_pk_bf16_f32 v20, v170, v171
	v_cvt_pk_bf16_f32 v21, v172, v173
	v_cvt_pk_bf16_f32 v22, v174, v175
	v_cvt_pk_bf16_f32 v23, v176, v177
	ds_write_b128 v24, v[20:23] offset:8192
	v_pk_mul_f32 v[178:179], v[178:179], s[44:45] op_sel_hi:[1,0]
	v_pk_mul_f32 v[180:181], v[180:181], s[44:45] op_sel_hi:[1,0]
	v_pk_mul_f32 v[182:183], v[182:183], s[44:45] op_sel_hi:[1,0]
	v_pk_mul_f32 v[184:185], v[184:185], s[44:45] op_sel_hi:[1,0]
	v_cvt_pk_bf16_f32 v12, v178, v179
	v_cvt_pk_bf16_f32 v13, v180, v181
	v_cvt_pk_bf16_f32 v14, v182, v183
	v_cvt_pk_bf16_f32 v15, v184, v185
	ds_write_b128 v25, v[12:15] offset:9216
	v_pk_mul_f32 v[186:187], v[186:187], s[44:45] op_sel_hi:[1,0]
	v_pk_mul_f32 v[188:189], v[188:189], s[44:45] op_sel_hi:[1,0]
	v_pk_mul_f32 v[190:191], v[190:191], s[44:45] op_sel_hi:[1,0]
	v_pk_mul_f32 v[192:193], v[192:193], s[44:45] op_sel_hi:[1,0]
	v_cvt_pk_bf16_f32 v16, v186, v187
	v_cvt_pk_bf16_f32 v17, v188, v189
	v_cvt_pk_bf16_f32 v18, v190, v191
	v_cvt_pk_bf16_f32 v19, v192, v193
	ds_write_b128 v24, v[16:19] offset:10240
	v_pk_mul_f32 v[194:195], v[194:195], s[44:45] op_sel_hi:[1,0]
	v_pk_mul_f32 v[196:197], v[196:197], s[44:45] op_sel_hi:[1,0]
	v_pk_mul_f32 v[198:199], v[198:199], s[44:45] op_sel_hi:[1,0]
	v_pk_mul_f32 v[200:201], v[200:201], s[44:45] op_sel_hi:[1,0]
	v_cvt_pk_bf16_f32 v20, v194, v195
	v_cvt_pk_bf16_f32 v21, v196, v197
	v_cvt_pk_bf16_f32 v22, v198, v199
	v_cvt_pk_bf16_f32 v23, v200, v201
	ds_write_b128 v25, v[20:23] offset:11264
	v_pk_mul_f32 v[42:43], v[42:43], s[44:45] op_sel_hi:[1,0]
	v_pk_mul_f32 v[44:45], v[44:45], s[44:45] op_sel_hi:[1,0]
	v_pk_mul_f32 v[46:47], v[46:47], s[44:45] op_sel_hi:[1,0]
	v_pk_mul_f32 v[48:49], v[48:49], s[44:45] op_sel_hi:[1,0]
	v_cvt_pk_bf16_f32 v12, v42, v43
	v_cvt_pk_bf16_f32 v13, v44, v45
	v_cvt_pk_bf16_f32 v14, v46, v47
	v_cvt_pk_bf16_f32 v15, v48, v49
	ds_write_b128 v24, v[12:15] offset:12288
	v_pk_mul_f32 v[50:51], v[50:51], s[44:45] op_sel_hi:[1,0]
	v_pk_mul_f32 v[52:53], v[52:53], s[44:45] op_sel_hi:[1,0]
	v_pk_mul_f32 v[54:55], v[54:55], s[44:45] op_sel_hi:[1,0]
	v_pk_mul_f32 v[56:57], v[56:57], s[44:45] op_sel_hi:[1,0]
	v_cvt_pk_bf16_f32 v16, v50, v51
	v_cvt_pk_bf16_f32 v17, v52, v53
	v_cvt_pk_bf16_f32 v18, v54, v55
	v_cvt_pk_bf16_f32 v19, v56, v57
	ds_write_b128 v25, v[16:19] offset:13312
	v_pk_mul_f32 v[58:59], v[58:59], s[44:45] op_sel_hi:[1,0]
	v_pk_mul_f32 v[60:61], v[60:61], s[44:45] op_sel_hi:[1,0]
	v_pk_mul_f32 v[62:63], v[62:63], s[44:45] op_sel_hi:[1,0]
	v_pk_mul_f32 v[64:65], v[64:65], s[44:45] op_sel_hi:[1,0]
	v_cvt_pk_bf16_f32 v20, v58, v59
	v_cvt_pk_bf16_f32 v21, v60, v61
	v_cvt_pk_bf16_f32 v22, v62, v63
	v_cvt_pk_bf16_f32 v23, v64, v65
	ds_write_b128 v24, v[20:23] offset:14336
	v_pk_mul_f32 v[66:67], v[66:67], s[44:45] op_sel_hi:[1,0]
	v_pk_mul_f32 v[68:69], v[68:69], s[44:45] op_sel_hi:[1,0]
	v_pk_mul_f32 v[70:71], v[70:71], s[44:45] op_sel_hi:[1,0]
	v_pk_mul_f32 v[72:73], v[72:73], s[44:45] op_sel_hi:[1,0]
	v_cvt_pk_bf16_f32 v12, v66, v67
	v_cvt_pk_bf16_f32 v13, v68, v69
	v_cvt_pk_bf16_f32 v14, v70, v71
	v_cvt_pk_bf16_f32 v15, v72, v73
	ds_write_b128 v25, v[12:15] offset:15360
	v_mov_b32_e32 v209, v41
	v_lshrrev_b32_e32 v29, 6, v0
	s_nop 0
	v_readfirstlane_b32 s50, v29
	s_mov_b32 s51, s30
	s_add_i32 s52, s24, s31
	s_mov_b32 s54, s32
	s_mov_b32 s55, s33
	s_lshl_b32 s43, s30, 16
	s_add_i32 s56, s43, 0x4000
	s_add_u32 s74, s34, 0x10000
	s_addc_u32 s75, s35, 0
	s_mov_b32 s76, s26
	s_mov_b32 s77, s27
	v_mov_b32_e32 v200, v4
	v_mov_b32_e32 v201, v5
	v_mov_b32_e32 v202, v6
	v_mov_b32_e32 v203, v7
	v_mov_b32_e32 v204, v8
	v_mov_b32_e32 v205, v9
	v_mov_b32_e32 v206, v10
	v_mov_b32_e32 v207, v11
	s_add_i32 s61, s28, s43
	s_add_i32 s43, s30, 1
	s_and_b32 s43, s43, 7
	s_lshl_b32 s43, s43, 16
	s_add_i32 s62, s28, s43
	s_add_i32 s43, s30, 2
	s_and_b32 s43, s43, 7
	s_lshl_b32 s43, s43, 16
	s_add_i32 s63, s28, s43
	s_add_i32 s43, s30, 3
	s_and_b32 s43, s43, 7
	s_lshl_b32 s43, s43, 16
	s_add_i32 s87, s28, s43
	s_add_i32 s43, s30, 7
	s_and_b32 s43, s43, 7
	s_lshl_b32 s43, s43, 16
	s_add_i32 s88, s28, s43
	s_add_i32 s88, s88, 0xc000
	s_mov_b32 s58, s87
	s_mov_b32 s57, s63
	s_mov_b32 s59, 0x10000
	s_mov_b32 s60, 0x10000
	s_lshl_b32 s43, s50, 11
	s_add_i32 s84, s43, 0x24000
	s_add_i32 s85, s84, 0x3f0
	s_mov_b32 s64, s10
	s_mov_b32 s65, s11
	s_mov_b32 s66, 0x10000
	s_mov_b32 s67, 0x4000
	s_mov_b32 s68, 0xc000
	s_mov_b32 s69, 0x14000
	s_mov_b32 s70, 0x600df1a6
	s_mov_b32 s71, 0x155510
	s_mov_b32 s72, s46
	s_mov_b32 s73, s47
	s_mov_b32 m0, s84
	s_nop 0
	buffer_load_dwordx4 v208, s[80:83], s86 offen lds
	s_mov_b32 m0, s85
	s_nop 0
	buffer_load_dwordx4 v208, s[80:83], s86 offen offset:16 lds
	s_add_i32 s86, s86, 0x2000
	s_mov_b32 s53, 0x10000
	s_waitcnt lgkmcnt(0)
	v_bfe_u32 v3, v0, 5, 1
	v_lshlrev_b32_e32 v4, 8, v0
	v_and_b32_e32 v4, 0x1f00, v4
	v_and_b32_e32 v5, 7, v0
	v_bitop3_b32 v6, v3, v0, 7 bitop3:0x78
	v_lshl_or_b32 v64, v6, 4, v4
	v_bitop3_b32 v6, v3, v5, 2 bitop3:0x36
	v_lshl_or_b32 v65, v6, 4, v4
	v_bitop3_b32 v6, v3, v5, 4 bitop3:0x36
	v_bitop3_b32 v5, v3, v5, 6 bitop3:0x36
	v_lshl_or_b32 v66, v6, 4, v4
	v_lshl_or_b32 v67, v5, 4, v4
	v_and_b32_e32 v4, 3, v0
	v_lshlrev_b32_e32 v6, 4, v0
	v_lshlrev_b32_e32 v5, 3, v4
	v_and_b32_e32 v6, 0xc0, v6
	v_lshlrev_b32_e32 v8, 1, v0
	v_lshlrev_b32_e32 v9, 8, v3
	v_bfe_u32 v7, v0, 4, 2
	v_and_b32_e32 v8, 32, v8
	v_or3_b32 v5, v5, v9, v6
	s_mov_b32 s0, 0x8000
	v_or3_b32 v184, v5, v8, s0
	v_lshlrev_b32_e32 v5, 8, v7
	v_xor_b32_e32 v6, v7, v1
	s_cmp_lg_u32 0, -1
	v_lshl_or_b32 v222, v6, 4, v5
	v_bitop3_b32 v1, v7, v1, 4 bitop3:0x36
	s_mov_b32 m0, s29
	s_nop 0
	buffer_load_dwordx4 v222, s[12:15], s61 offen lds
	s_cselect_b32 s17, 0, 0
	v_lshl_or_b32 v223, v1, 4, v5
	s_add_i32 s20, s29, 0x400
	s_add_i32 s0, s61, 0x400
	s_mov_b32 m0, s20
	s_nop 0
	buffer_load_dwordx4 v223, s[12:15], s0 offen lds
	v_lshlrev_b32_e32 v0, 6, v0
	s_add_i32 s21, s29, 0x800
	s_add_i32 s0, s61, 0x800
	s_mov_b32 m0, s21
	s_nop 0
	buffer_load_dwordx4 v222, s[12:15], s0 offen lds
	v_and_b32_e32 v0, 0x700, v0
	v_lshlrev_b32_e32 v1, 6, v3
	v_lshlrev_b32_e32 v3, 4, v4
	s_add_i32 s22, s29, 0xc00
	s_add_i32 s1, s61, 0xc00
	s_mov_b32 m0, s22
	s_nop 0
	buffer_load_dwordx4 v223, s[12:15], s1 offen lds
	v_or3_b32 v196, v0, v1, v3
	s_add_i32 s2, s29, 0x8000
	s_mov_b32 m0, s2
	s_nop 0
	buffer_load_dwordx4 v196, s[4:7], s61 offen lds
	s_add_i32 s1, s2, 0x400
	s_add_i32 s3, s61, 0x80
	s_mov_b32 m0, s1
	s_nop 0
	buffer_load_dwordx4 v196, s[4:7], s3 offen lds
	s_add_i32 s1, s2, 0x800
	s_mov_b32 m0, s1
	s_nop 0
	buffer_load_dwordx4 v196, s[4:7], s0 offen lds
	s_add_i32 s0, s2, 0xc00
	s_add_i32 s1, s61, 0x880
	s_mov_b32 m0, s0
	s_nop 0
	buffer_load_dwordx4 v196, s[4:7], s1 offen lds
	v_or_b32_e32 v2, 0x10000, v40
	v_add_u32_e32 v218, s17, v64
	v_add_u32_e32 v219, s17, v65
	v_add_u32_e32 v220, s17, v66
	v_add_u32_e32 v221, s17, v67
	v_add_u32_e32 v32, v2, v218
	v_add_u32_e32 v33, v2, v219
	v_add_u32_e32 v34, v2, v220
	v_add_u32_e32 v35, v2, v221
	v_add_u32_e32 v212, s17, v184
	ds_read_b128 v[0:3], v32 offset:0
	ds_read_b128 v[4:7], v33 offset:0
	ds_read_b128 v[8:11], v34 offset:0
	ds_read_b128 v[12:15], v35 offset:0
	ds_read_b128 v[16:19], v32 offset:128
	ds_read_b128 v[20:23], v33 offset:128
	ds_read_b128 v[24:27], v34 offset:128
	ds_read_b128 v[28:31], v35 offset:128
	s_waitcnt lgkmcnt(0)
	v_accvgpr_write_b32 a[128], v0
	v_accvgpr_write_b32 a[129], v1
	v_accvgpr_write_b32 a[130], v2
	v_accvgpr_write_b32 a[131], v3
	v_accvgpr_write_b32 a[132], v4
	v_accvgpr_write_b32 a[133], v5
	v_accvgpr_write_b32 a[134], v6
	v_accvgpr_write_b32 a[135], v7
	v_accvgpr_write_b32 a[136], v8
	v_accvgpr_write_b32 a[137], v9
	v_accvgpr_write_b32 a[138], v10
	v_accvgpr_write_b32 a[139], v11
	v_accvgpr_write_b32 a[140], v12
	v_accvgpr_write_b32 a[141], v13
	v_accvgpr_write_b32 a[142], v14
	v_accvgpr_write_b32 a[143], v15
	v_accvgpr_write_b32 a[144], v16
	v_accvgpr_write_b32 a[145], v17
	v_accvgpr_write_b32 a[146], v18
	v_accvgpr_write_b32 a[147], v19
	v_accvgpr_write_b32 a[148], v20
	v_accvgpr_write_b32 a[149], v21
	v_accvgpr_write_b32 a[150], v22
	v_accvgpr_write_b32 a[151], v23
	v_accvgpr_write_b32 a[152], v24
	v_accvgpr_write_b32 a[153], v25
	v_accvgpr_write_b32 a[154], v26
	v_accvgpr_write_b32 a[155], v27
	v_accvgpr_write_b32 a[156], v28
	v_accvgpr_write_b32 a[157], v29
	v_accvgpr_write_b32 a[158], v30
	v_accvgpr_write_b32 a[159], v31
	ds_read_b128 v[0:3], v32 offset:8192
	ds_read_b128 v[4:7], v33 offset:8192
	ds_read_b128 v[8:11], v34 offset:8192
	ds_read_b128 v[12:15], v35 offset:8192
	ds_read_b128 v[16:19], v32 offset:8320
	ds_read_b128 v[20:23], v33 offset:8320
	ds_read_b128 v[24:27], v34 offset:8320
	ds_read_b128 v[28:31], v35 offset:8320
	s_waitcnt lgkmcnt(0)
	v_accvgpr_write_b32 a[160], v0
	v_accvgpr_write_b32 a[161], v1
	v_accvgpr_write_b32 a[162], v2
	v_accvgpr_write_b32 a[163], v3
	v_accvgpr_write_b32 a[164], v4
	v_accvgpr_write_b32 a[165], v5
	v_accvgpr_write_b32 a[166], v6
	v_accvgpr_write_b32 a[167], v7
	v_accvgpr_write_b32 a[168], v8
	v_accvgpr_write_b32 a[169], v9
	v_accvgpr_write_b32 a[170], v10
	v_accvgpr_write_b32 a[171], v11
	v_accvgpr_write_b32 a[172], v12
	v_accvgpr_write_b32 a[173], v13
	v_accvgpr_write_b32 a[174], v14
	v_accvgpr_write_b32 a[175], v15
	v_accvgpr_write_b32 a[176], v16
	v_accvgpr_write_b32 a[177], v17
	v_accvgpr_write_b32 a[178], v18
	v_accvgpr_write_b32 a[179], v19
	v_accvgpr_write_b32 a[180], v20
	v_accvgpr_write_b32 a[181], v21
	v_accvgpr_write_b32 a[182], v22
	v_accvgpr_write_b32 a[183], v23
	v_accvgpr_write_b32 a[184], v24
	v_accvgpr_write_b32 a[185], v25
	v_accvgpr_write_b32 a[186], v26
	v_accvgpr_write_b32 a[187], v27
	v_accvgpr_write_b32 a[188], v28
	v_accvgpr_write_b32 a[189], v29
	v_accvgpr_write_b32 a[190], v30
	v_accvgpr_write_b32 a[191], v31
	s_waitcnt vmcnt(0) lgkmcnt(0)
	s_barrier
	s_nop 0
	ds_read_b128 a[192:195], v218 offset:0
	s_nop 0
	ds_read_b128 a[196:199], v219 offset:0
	ds_read_b128 a[200:203], v220 offset:0
	ds_read_b128 a[204:207], v221 offset:0
	ds_read_b128 a[208:211], v218 offset:128
	ds_read_b128 a[212:215], v219 offset:128
	ds_read_b128 a[216:219], v220 offset:128
	ds_read_b128 a[220:223], v221 offset:128
	ds_read_b128 a[224:227], v218 offset:8192
	ds_read_b128 a[228:231], v219 offset:8192
	ds_read_b128 a[232:235], v220 offset:8192
	ds_read_b128 a[236:239], v221 offset:8192
	ds_read_b128 a[240:243], v218 offset:8320
	ds_read_b128 a[244:247], v219 offset:8320
	ds_read_b128 a[248:251], v220 offset:8320
	ds_read_b128 a[252:255], v221 offset:8320
	s_waitcnt lgkmcnt(0)
	s_waitcnt vmcnt(0)
	v_cmp_eq_u32_e32 vcc, s70, v38
	s_cmp_eq_u64 vcc, exec
	s_cbranch_scc0 .LBB0_27
.LBB0_11:
	s_add_i32 s3, s29, 0x4000
	s_add_i32 s19, s62, 0x0
	s_mov_b32 m0, s3
	s_nop 0
	buffer_load_dwordx4 v222, s[12:15], s19 offen lds
	s_add_i32 s10, s29, 0x4400
	s_add_i32 s0, s62, 0x400
	s_mov_b32 m0, s10
	s_nop 0
	buffer_load_dwordx4 v223, s[12:15], s0 offen lds
	s_add_i32 s11, s29, 0x4800
	s_add_i32 s18, s62, 0x800
	s_mov_b32 m0, s11
	s_nop 0
	buffer_load_dwordx4 v222, s[12:15], s18 offen lds
	s_add_i32 s16, s29, 0x4c00
	s_add_i32 s0, s62, 0xc00
	s_mov_b32 m0, s16
	s_nop 0
	buffer_load_dwordx4 v223, s[12:15], s0 offen lds
	v_mfma_f32_32x32x16_bf16 v[48:63], a[192:195], a[128:131], 0
	v_mfma_f32_32x32x16_bf16 v[32:47], a[192:195], a[160:163], 0
	v_mfma_f32_32x32x16_bf16 v[0:15], a[224:227], a[128:131], 0
	v_mfma_f32_32x32x16_bf16 v[16:31], a[224:227], a[160:163], 0
	v_mfma_f32_32x32x16_bf16 v[48:63], a[196:199], a[132:135], v[48:63]
	v_mfma_f32_32x32x16_bf16 v[32:47], a[196:199], a[164:167], v[32:47]
	v_mfma_f32_32x32x16_bf16 v[0:15], a[228:231], a[132:135], v[0:15]
	v_mfma_f32_32x32x16_bf16 v[16:31], a[228:231], a[164:167], v[16:31]
	v_mfma_f32_32x32x16_bf16 v[48:63], a[200:203], a[136:139], v[48:63]
	v_mfma_f32_32x32x16_bf16 v[32:47], a[200:203], a[168:171], v[32:47]
	v_mfma_f32_32x32x16_bf16 v[0:15], a[232:235], a[136:139], v[0:15]
	v_mfma_f32_32x32x16_bf16 v[16:31], a[232:235], a[168:171], v[16:31]
	v_mfma_f32_32x32x16_bf16 v[48:63], a[204:207], a[140:143], v[48:63]
	v_mfma_f32_32x32x16_bf16 v[32:47], a[204:207], a[172:175], v[32:47]
	v_mfma_f32_32x32x16_bf16 v[0:15], a[236:239], a[140:143], v[0:15]
	v_mfma_f32_32x32x16_bf16 v[16:31], a[236:239], a[172:175], v[16:31]
	v_mfma_f32_32x32x16_bf16 v[48:63], a[208:211], a[144:147], v[48:63]
	s_mov_b32 s27, s29
	v_mfma_f32_32x32x16_bf16 v[32:47], a[208:211], a[176:179], v[32:47]
	s_add_i32 s0, s63, 0x0
	s_mov_b32 s30, s0
	v_mfma_f32_32x32x16_bf16 v[0:15], a[240:243], a[144:147], v[0:15]
	s_mov_b32 s31, s20
	v_mfma_f32_32x32x16_bf16 v[16:31], a[240:243], a[176:179], v[16:31]
	s_add_i32 s33, s63, 0x400
	v_mfma_f32_32x32x16_bf16 v[48:63], a[212:215], a[148:151], v[48:63]
	s_mov_b32 s34, s21
	v_mfma_f32_32x32x16_bf16 v[32:47], a[212:215], a[180:183], v[32:47]
	s_add_i32 s1, s63, 0x800
	s_mov_b32 s35, s1
	v_mfma_f32_32x32x16_bf16 v[0:15], a[244:247], a[148:151], v[0:15]
	s_mov_b32 s36, s22
	v_mfma_f32_32x32x16_bf16 v[16:31], a[244:247], a[180:183], v[16:31]
	s_add_i32 s37, s63, 0xc00
	v_mfma_f32_32x32x16_bf16 v[48:63], a[216:219], a[152:155], v[48:63]
	s_add_i32 s23, s29, 0xc000
	s_mov_b32 s38, s23
	v_mfma_f32_32x32x16_bf16 v[32:47], a[216:219], a[184:187], v[32:47]
	v_mfma_f32_32x32x16_bf16 v[0:15], a[248:251], a[152:155], v[0:15]
	s_add_i32 s24, s29, 0xc400
	s_mov_b32 s39, s24
	v_mfma_f32_32x32x16_bf16 v[16:31], a[248:251], a[184:187], v[16:31]
	s_add_i32 s40, s62, 0x80
	v_mfma_f32_32x32x16_bf16 v[48:63], a[220:223], a[156:159], v[48:63]
	s_add_i32 s25, s29, 0xc800
	s_mov_b32 s41, s25
	v_mfma_f32_32x32x16_bf16 v[32:47], a[220:223], a[188:191], v[32:47]
	v_mfma_f32_32x32x16_bf16 v[0:15], a[252:255], a[156:159], v[0:15]
	s_add_i32 s26, s29, 0xcc00
	s_mov_b32 s42, s26
	v_mfma_f32_32x32x16_bf16 v[16:31], a[252:255], a[188:191], v[16:31]
	s_add_i32 s43, s62, 0x880
	s_waitcnt vmcnt(0) lgkmcnt(0)
	s_barrier
	s_nop 0
	s_mov_b32 m0, s27
	s_nop 0
	buffer_load_dwordx4 v222, s[12:15], s30 offen lds
	s_mov_b32 m0, s31
	s_nop 0
	buffer_load_dwordx4 v223, s[12:15], s33 offen lds
	s_addk_i32 s17, 0x4000
	v_add_u32_e32 v217, s17, v64
	ds_read_b128 a[192:195], v217 offset:0
	s_mov_b32 m0, s34
	s_nop 0
	buffer_load_dwordx4 v222, s[12:15], s35 offen lds
	v_add_u32_e32 v199, s17, v65
	ds_read_b128 a[196:199], v199 offset:0
	s_mov_b32 m0, s36
	s_nop 0
	buffer_load_dwordx4 v223, s[12:15], s37 offen lds
	v_add_u32_e32 v198, s17, v66
	ds_read_b128 a[200:203], v198 offset:0
	s_mov_b32 m0, s38
	s_nop 0
	buffer_load_dwordx4 v196, s[4:7], s19 offen lds
	v_add_u32_e32 v197, s17, v67
	ds_read_b128 a[204:207], v197 offset:0
	s_mov_b32 m0, s39
	s_nop 0
	buffer_load_dwordx4 v196, s[4:7], s40 offen lds
	ds_read_b128 a[208:211], v217 offset:128
	s_mov_b32 m0, s41
	s_nop 0
	buffer_load_dwordx4 v196, s[4:7], s18 offen lds
	ds_read_b128 a[212:215], v199 offset:128
	s_mov_b32 m0, s42
	s_nop 0
	buffer_load_dwordx4 v196, s[4:7], s43 offen lds
	ds_read_b128 a[216:219], v198 offset:128
	ds_read_b128 a[220:223], v197 offset:128
	v_cvt_pk_bf16_f32 v248, v248, v249
	v_cvt_pk_bf16_f32 v249, v250, v251
	v_cvt_pk_bf16_f32 v250, v252, v253
	v_cvt_pk_bf16_f32 v251, v254, v255
	v_lshrrev_b32_e32 v252, 1, v208
	buffer_store_dwordx4 v[248:251], v252, s[12:15], s56 offen sc1
	v_mbcnt_lo_u32_b32 v253, -1, 0
	v_mbcnt_hi_u32_b32 v253, -1, v253
	v_lshlrev_b32_e32 v253, 4, v253
	v_add_u32_e32 v253, s84, v253
	ds_read_b128 v[248:251], v253
	ds_read_b128 v[252:255], v253 offset:1024
	v_max3_f32 v64, v48, v49, v0
	v_max3_f32 v65, v50, v51, v1
	v_max3_f32 v64, v64, v2, v3
	ds_read_b128 a[224:227], v217 offset:8192
	v_max3_f32 v64, v64, v52, v53
	v_max3_f32 v65, v65, v54, v55
	v_max3_f32 v64, v64, v4, v5
	v_max3_f32 v65, v65, v6, v7
	ds_read_b128 a[228:231], v199 offset:8192
	v_max3_f32 v64, v64, v56, v57
	v_max3_f32 v65, v65, v58, v59
	v_max3_f32 v64, v64, v8, v9
	v_max3_f32 v65, v65, v10, v11
	ds_read_b128 a[232:235], v198 offset:8192
	v_max3_f32 v64, v64, v60, v61
	v_max3_f32 v65, v65, v62, v63
	v_max3_f32 v64, v64, v12, v13
	v_max3_f32 v65, v65, v14, v15
	ds_read_b128 a[236:239], v197 offset:8192
	v_max3_f32 v66, v32, v33, v16
	v_max3_f32 v67, v34, v35, v17
	v_max3_f32 v66, v66, v18, v19
	ds_read_b128 a[240:243], v217 offset:8320
	v_max3_f32 v66, v66, v36, v37
	v_max3_f32 v67, v67, v38, v39
	v_max3_f32 v66, v66, v20, v21
	v_max3_f32 v67, v67, v22, v23
	ds_read_b128 a[244:247], v199 offset:8320
	v_max3_f32 v66, v66, v40, v41
	v_max3_f32 v67, v67, v42, v43
	v_max3_f32 v66, v66, v24, v25
	v_max3_f32 v67, v67, v26, v27
	ds_read_b128 a[248:251], v198 offset:8320
	v_max3_f32 v66, v66, v44, v45
	v_max3_f32 v67, v67, v46, v47
	v_max3_f32 v66, v66, v28, v29
	v_max3_f32 v67, v67, v30, v31
	ds_read_b128 a[252:255], v197 offset:8320
	s_waitcnt lgkmcnt(8)
	v_pk_add_f32 v[200:201], v[248:249], v[200:201]
	v_pk_add_f32 v[202:203], v[250:251], v[202:203]
	v_pk_add_f32 v[204:205], v[252:253], v[204:205]
	v_pk_add_f32 v[206:207], v[254:255], v[206:207]
	v_cvt_pk_bf16_f32 v248, v248, v249
	v_cvt_pk_bf16_f32 v249, v250, v251
	v_cvt_pk_bf16_f32 v250, v252, v253
	v_cvt_pk_bf16_f32 v251, v254, v255
	v_lshrrev_b32_e32 v252, 1, v208
	buffer_store_dwordx4 v[248:251], v252, s[4:7], s56 offen sc1
	s_add_i32 s56, s56, 0x1000
	s_nop 1
	global_load_dwordx4 v[248:251], v208, s[54:55] nt
	global_load_dwordx4 v[252:255], v208, s[54:55] offset:16 nt
	s_add_u32 s54, s54, 0x2000
	s_addc_u32 s55, s55, 0
	s_mov_b32 m0, s84
	s_nop 0
	buffer_load_dwordx4 v208, s[80:83], s86 offen lds
	s_mov_b32 m0, s85
	s_nop 0
	buffer_load_dwordx4 v208, s[80:83], s86 offen offset:16 lds
	s_add_i32 s86, s86, 0x2000
	v_max_f32_e32 v64, v64, v65
	v_mov_b32_e32 v65, v64
	s_nop 1
	v_permlane32_swap_b32_e32 v64, v65
	v_max_f32_e32 v214, v64, v65
	v_max_f32_e32 v64, v66, v67
	v_mov_b32_e32 v65, v64
	s_nop 1
	v_permlane32_swap_b32_e32 v64, v65
	v_max_f32_e32 v213, v64, v65
	v_sub_f32_e32 v64, v0, v214
	v_mbcnt_lo_u32_b32 v0, -1, 0
	v_mbcnt_hi_u32_b32 v0, -1, v0
	v_sub_f32_e32 v65, v1, v214
	v_xor_b32_e32 v1, 0x80000000, v214
	v_cmp_gt_u32_e32 vcc, 32, v0
	v_sub_f32_e32 v128, v2, v214
	v_sub_f32_e32 v129, v3, v214
	v_sub_f32_e32 v130, v4, v214
	v_sub_f32_e32 v131, v5, v214
	v_sub_f32_e32 v132, v6, v214
	v_sub_f32_e32 v133, v7, v214
	v_sub_f32_e32 v134, v8, v214
	v_sub_f32_e32 v135, v9, v214
	v_sub_f32_e32 v136, v10, v214
	v_sub_f32_e32 v137, v11, v214
	v_sub_f32_e32 v138, v12, v214
	v_sub_f32_e32 v139, v13, v214
	v_sub_f32_e32 v140, v14, v214
	v_sub_f32_e32 v141, v15, v214
	v_sub_f32_e32 v142, v16, v213
	v_mov_b32_e32 v211, 1.0
	v_sub_f32_e32 v143, v17, v213
	v_xor_b32_e32 v17, 0x80000000, v213
	v_cndmask_b32_e64 v0, 0, 1.0, vcc
	s_nop 1
	v_mfma_f32_32x32x2_f32 v[0:15], v0, v1, 0
	v_mbcnt_lo_u32_b32 v16, -1, 0
	v_mbcnt_hi_u32_b32 v16, -1, v16
	v_sub_f32_e32 v48, v48, v214
	v_sub_f32_e32 v49, v49, v214
	v_sub_f32_e32 v50, v50, v214
	v_sub_f32_e32 v51, v51, v214
	v_sub_f32_e32 v52, v52, v214
	v_sub_f32_e32 v53, v53, v214
	v_sub_f32_e32 v54, v54, v214
	v_sub_f32_e32 v55, v55, v214
	v_sub_f32_e32 v56, v56, v214
	v_sub_f32_e32 v57, v57, v214
	v_sub_f32_e32 v58, v58, v214
	v_sub_f32_e32 v59, v59, v214
	v_sub_f32_e32 v60, v60, v214
	v_sub_f32_e32 v61, v61, v214
	v_sub_f32_e32 v62, v62, v214
	v_sub_f32_e32 v63, v63, v214
	v_sub_f32_e32 v32, v32, v213
	v_sub_f32_e32 v33, v33, v213
	v_sub_f32_e32 v34, v34, v213
	v_cmp_gt_u32_e32 vcc, 32, v16
	v_sub_f32_e32 v35, v35, v213
	v_sub_f32_e32 v36, v36, v213
	v_sub_f32_e32 v37, v37, v213
	v_sub_f32_e32 v38, v38, v213
	v_sub_f32_e32 v39, v39, v213
	v_sub_f32_e32 v40, v40, v213
	v_sub_f32_e32 v41, v41, v213
	v_sub_f32_e32 v42, v42, v213
	v_sub_f32_e32 v43, v43, v213
	v_sub_f32_e32 v44, v44, v213
	v_sub_f32_e32 v45, v45, v213
	v_sub_f32_e32 v46, v46, v213
	v_sub_f32_e32 v47, v47, v213
	v_sub_f32_e32 v144, v18, v213
	v_sub_f32_e32 v145, v19, v213
	v_sub_f32_e32 v146, v20, v213
	v_sub_f32_e32 v147, v21, v213
	v_sub_f32_e32 v183, v22, v213
	v_sub_f32_e32 v194, v23, v213
	v_cndmask_b32_e64 v16, 0, 1.0, vcc
	v_sub_f32_e32 v195, v24, v213
	v_sub_f32_e32 v215, v25, v213
	v_sub_f32_e32 v216, v26, v213
	v_sub_f32_e32 v224, v27, v213
	v_sub_f32_e32 v225, v28, v213
	v_sub_f32_e32 v226, v29, v213
	v_sub_f32_e32 v229, v30, v213
	v_sub_f32_e32 v230, v31, v213
	v_mfma_f32_32x32x2_f32 v[16:31], v16, v17, 0
	v_exp_f32_e32 v112, v48
	v_exp_f32_e32 v113, v49
	v_exp_f32_e32 v114, v50
	v_exp_f32_e32 v115, v51
	v_mov_b32_e32 v193, 0
	v_add_f32_e32 v48, v193, v112
	v_add_f32_e32 v49, v193, v113
	v_exp_f32_e32 v116, v52
	v_exp_f32_e32 v117, v53
	v_exp_f32_e32 v118, v54
	v_add_f32_e32 v48, v48, v114
	v_add_f32_e32 v49, v49, v115
	v_exp_f32_e32 v119, v55
	v_exp_f32_e32 v120, v56
	v_add_f32_e32 v48, v48, v116
	v_add_f32_e32 v49, v49, v117
	v_add_f32_e32 v48, v48, v118
	v_exp_f32_e32 v121, v57
	v_exp_f32_e32 v122, v58
	v_exp_f32_e32 v123, v59
	v_add_f32_e32 v49, v49, v119
	v_add_f32_e32 v48, v48, v120
	v_exp_f32_e32 v124, v60
	v_exp_f32_e32 v125, v61
	v_add_f32_e32 v49, v49, v121
	v_add_f32_e32 v48, v48, v122
	v_add_f32_e32 v49, v49, v123
	v_exp_f32_e32 v126, v62
	v_exp_f32_e32 v127, v63
	v_exp_f32_e32 v96, v32
	v_add_f32_e32 v32, v48, v124
	v_add_f32_e32 v48, v49, v125
	v_exp_f32_e32 v97, v33
	v_exp_f32_e32 v98, v34
	v_add_f32_e32 v231, v32, v126
	v_add_f32_e32 v232, v48, v127
	v_add_f32_e32 v32, v193, v96
	v_exp_f32_e32 v99, v35
	v_exp_f32_e32 v100, v36
	v_exp_f32_e32 v101, v37
	v_add_f32_e32 v33, v193, v97
	v_add_f32_e32 v32, v32, v98
	v_exp_f32_e32 v102, v38
	v_exp_f32_e32 v103, v39
	v_add_f32_e32 v33, v33, v99
	v_add_f32_e32 v32, v32, v100
	v_add_f32_e32 v33, v33, v101
	v_exp_f32_e32 v104, v40
	v_exp_f32_e32 v105, v41
	v_exp_f32_e32 v106, v42
	v_add_f32_e32 v32, v32, v102
	v_add_f32_e32 v33, v33, v103
	v_exp_f32_e32 v107, v43
	v_exp_f32_e32 v108, v44
	v_add_f32_e32 v32, v32, v104
	v_add_f32_e32 v33, v33, v105
	v_add_f32_e32 v32, v32, v106
	v_exp_f32_e32 v109, v45
	v_exp_f32_e32 v110, v46
	v_exp_f32_e32 v111, v47
	v_add_f32_e32 v33, v33, v107
	v_add_f32_e32 v32, v32, v108
	s_waitcnt lgkmcnt(0)
	v_add_f32_e32 v33, v33, v109
	v_add_f32_e32 v233, v32, v110
	v_add_f32_e32 v234, v33, v111
	v_mfma_f32_32x32x16_bf16 v[80:95], a[192:195], a[128:131], v[0:15]
	ds_read_b64_tr_b16 v[160:161], v212 offset:0
	v_exp_f32_e32 v235, v64
	v_exp_f32_e32 v236, v65
	v_cvt_pk_bf16_f32 v152, v112, v113
	v_mfma_f32_32x32x16_bf16 v[64:79], a[192:195], a[160:163], v[16:31]
	ds_read_b64_tr_b16 v[162:163], v212 offset:0x800
	v_exp_f32_e32 v237, v128
	v_exp_f32_e32 v238, v129
	v_cvt_pk_bf16_f32 v153, v114, v115
	v_exp_f32_e32 v115, v130
	v_mfma_f32_32x32x16_bf16 v[48:63], a[224:227], a[128:131], v[0:15]
	ds_read_b64_tr_b16 v[172:173], v212 offset:0x200
	v_exp_f32_e32 v239, v131
	v_cvt_pk_bf16_f32 v154, v116, v117
	v_mfma_f32_32x32x16_bf16 v[32:47], a[224:227], a[160:163], v[16:31]
	ds_read_b64_tr_b16 v[174:175], v212 offset:0xa00
	ds_read_b64_tr_b16 v[168:169], v212 offset:0x400
	v_exp_f32_e32 v240, v132
	v_exp_f32_e32 v241, v133
	v_cvt_pk_bf16_f32 v155, v118, v119
	v_exp_f32_e32 v185, v134
	v_exp_f32_e32 v186, v135
	v_mfma_f32_32x32x16_bf16 v[80:95], a[196:199], a[132:135], v[80:95]
	ds_read_b64_tr_b16 v[170:171], v212 offset:0xc00
	v_cvt_pk_bf16_f32 v128, v120, v121
	v_exp_f32_e32 v187, v136
	v_exp_f32_e32 v188, v137
	v_mfma_f32_32x32x16_bf16 v[64:79], a[196:199], a[164:167], v[64:79]
	ds_read_b64_tr_b16 v[176:177], v212 offset:0x600
	v_cvt_pk_bf16_f32 v129, v122, v123
	v_exp_f32_e32 v189, v138
	v_exp_f32_e32 v190, v139
	v_mfma_f32_32x32x16_bf16 v[48:63], a[228:231], a[132:135], v[48:63]
	ds_read_b64_tr_b16 v[178:179], v212 offset:0xe00
	v_cvt_pk_bf16_f32 v130, v124, v125
	v_mfma_f32_32x32x16_bf16 v[32:47], a[228:231], a[164:167], v[32:47]
	ds_read_b64_tr_b16 v[164:165], v212 offset:0x1000
	v_exp_f32_e32 v191, v140
	v_exp_f32_e32 v192, v141
	ds_read_b64_tr_b16 v[166:167], v212 offset:0x1800
	v_cvt_pk_bf16_f32 v131, v126, v127
	v_exp_f32_e32 v141, v142
	v_exp_f32_e32 v142, v143
	v_mfma_f32_32x32x16_bf16 v[80:95], a[200:203], a[136:139], v[80:95]
	ds_read_b64_tr_b16 v[156:157], v212 offset:0x1200
	v_cvt_pk_bf16_f32 v180, v96, v97
	v_exp_f32_e32 v143, v144
	v_mfma_f32_32x32x16_bf16 v[64:79], a[200:203], a[168:171], v[64:79]
	ds_read_b64_tr_b16 v[158:159], v212 offset:0x1a00
	v_exp_f32_e32 v242, v145
	v_cvt_pk_bf16_f32 v181, v98, v99
	v_mfma_f32_32x32x16_bf16 v[48:63], a[232:235], a[136:139], v[48:63]
	ds_read_b64_tr_b16 v[148:149], v212 offset:0x1400
	v_exp_f32_e32 v243, v146
	v_exp_f32_e32 v244, v147
	v_cvt_pk_bf16_f32 v182, v100, v101
	v_mfma_f32_32x32x16_bf16 v[32:47], a[232:235], a[168:171], v[32:47]
	ds_read_b64_tr_b16 v[150:151], v212 offset:0x1c00
	ds_read_b64_tr_b16 v[136:137], v212 offset:0x1600
	v_exp_f32_e32 v245, v183
	v_exp_f32_e32 v246, v194
	v_cvt_pk_bf16_f32 v183, v102, v103
	v_exp_f32_e32 v194, v195
	v_exp_f32_e32 v195, v215
	v_mfma_f32_32x32x16_bf16 v[80:95], a[204:207], a[140:143], v[80:95]
	ds_read_b64_tr_b16 v[138:139], v212 offset:0x1e00
	v_cvt_pk_bf16_f32 v144, v104, v105
	v_exp_f32_e32 v215, v216
	v_exp_f32_e32 v224, v224
	v_mfma_f32_32x32x16_bf16 v[64:79], a[204:207], a[172:175], v[64:79]
	ds_read_b64_tr_b16 v[132:133], v212 offset:0x2000
	v_cvt_pk_bf16_f32 v145, v106, v107
	v_exp_f32_e32 v227, v225
	v_exp_f32_e32 v228, v226
	v_mfma_f32_32x32x16_bf16 v[48:63], a[236:239], a[140:143], v[48:63]
	ds_read_b64_tr_b16 v[134:135], v212 offset:0x2800
	v_cvt_pk_bf16_f32 v146, v108, v109
	v_mfma_f32_32x32x16_bf16 v[32:47], a[236:239], a[172:175], v[32:47]
	ds_read_b64_tr_b16 v[124:125], v212 offset:0x2200
	v_exp_f32_e32 v229, v229
	v_exp_f32_e32 v230, v230
	ds_read_b64_tr_b16 v[126:127], v212 offset:0x2a00
	v_cvt_pk_bf16_f32 v147, v110, v111
	s_mov_b32 s27, s3
	v_mfma_f32_32x32x16_bf16 v[80:95], a[208:211], a[144:147], v[80:95]
	ds_read_b64_tr_b16 v[120:121], v212 offset:0x2400
	v_cvt_pk_bf16_f32 v112, v235, v236
	v_add_f32_e32 v96, v231, v235
	v_add_f32_e32 v97, v232, v236
	s_add_i32 s30, s87, 0x0
	v_mfma_f32_32x32x16_bf16 v[64:79], a[208:211], a[176:179], v[64:79]
	ds_read_b64_tr_b16 v[122:123], v212 offset:0x2c00
	v_cvt_pk_bf16_f32 v113, v237, v238
	v_add_f32_e32 v96, v96, v237
	v_add_f32_e32 v97, v97, v238
	s_mov_b32 s31, s10
	v_mfma_f32_32x32x16_bf16 v[48:63], a[240:243], a[144:147], v[48:63]
	ds_read_b64_tr_b16 v[116:117], v212 offset:0x2600
	v_cvt_pk_bf16_f32 v114, v115, v239
	v_add_f32_e32 v96, v96, v115
	v_add_f32_e32 v97, v97, v239
	s_add_i32 s33, s87, 0x400
	v_mfma_f32_32x32x16_bf16 v[32:47], a[240:243], a[176:179], v[32:47]
	ds_read_b64_tr_b16 v[118:119], v212 offset:0x2e00
	ds_read_b64_tr_b16 v[104:105], v212 offset:0x3000
	v_cvt_pk_bf16_f32 v115, v240, v241
	v_add_f32_e32 v96, v96, v240
	v_add_f32_e32 v97, v97, v241
	s_mov_b32 s34, s11
	v_mfma_f32_32x32x16_bf16 v[80:95], a[212:215], a[148:151], v[80:95]
	ds_read_b64_tr_b16 v[106:107], v212 offset:0x3800
	v_add_f32_e32 v96, v96, v185
	v_add_f32_e32 v97, v97, v186
	s_add_i32 s35, s87, 0x800
	v_mfma_f32_32x32x16_bf16 v[64:79], a[212:215], a[180:183], v[64:79]
	ds_read_b64_tr_b16 v[108:109], v212 offset:0x3200
	v_add_f32_e32 v96, v96, v187
	v_add_f32_e32 v97, v97, v188
	s_mov_b32 s36, s16
	v_mfma_f32_32x32x16_bf16 v[48:63], a[244:247], a[148:151], v[48:63]
	ds_read_b64_tr_b16 v[110:111], v212 offset:0x3a00
	v_add_f32_e32 v96, v96, v189
	v_add_f32_e32 v97, v97, v190
	s_add_i32 s37, s87, 0xc00
	v_mfma_f32_32x32x16_bf16 v[32:47], a[244:247], a[180:183], v[32:47]
	ds_read_b64_tr_b16 v[100:101], v212 offset:0x3400
	ds_read_b64_tr_b16 v[102:103], v212 offset:0x3c00
	v_add_f32_e32 v216, v96, v191
	v_add_f32_e32 v225, v97, v192
	s_mov_b32 s38, s2
	v_mfma_f32_32x32x16_bf16 v[80:95], a[216:219], a[152:155], v[80:95]
	ds_read_b64_tr_b16 v[96:97], v212 offset:0x3600
	v_cvt_pk_bf16_f32 v140, v141, v142
	v_add_f32_e32 v226, v233, v141
	v_add_f32_e32 v142, v234, v142
	v_mfma_f32_32x32x16_bf16 v[64:79], a[216:219], a[184:187], v[64:79]
	ds_read_b64_tr_b16 v[98:99], v212 offset:0x3e00
	v_cvt_pk_bf16_f32 v141, v143, v242
	v_add_f32_e32 v143, v226, v143
	v_add_f32_e32 v226, v142, v242
	v_mfma_f32_32x32x16_bf16 v[48:63], a[248:251], a[152:155], v[48:63]
	s_add_i32 s17, s29, 0x8400
	s_mov_b32 s39, s17
	v_cvt_pk_bf16_f32 v142, v243, v244
	v_add_f32_e32 v231, v143, v243
	v_add_f32_e32 v226, v226, v244
	v_mfma_f32_32x32x16_bf16 v[32:47], a[248:251], a[184:187], v[32:47]
	s_add_i32 s40, s63, 0x80
	v_cvt_pk_bf16_f32 v143, v245, v246
	v_add_f32_e32 v231, v231, v245
	v_add_f32_e32 v226, v226, v246
	v_mfma_f32_32x32x16_bf16 v[80:95], a[220:223], a[156:159], v[80:95]
	s_add_i32 s18, s29, 0x8800
	s_mov_b32 s41, s18
	v_add_f32_e32 v231, v231, v194
	v_add_f32_e32 v226, v226, v195
	v_mfma_f32_32x32x16_bf16 v[64:79], a[220:223], a[188:191], v[64:79]
	v_add_f32_e32 v231, v231, v215
	v_add_f32_e32 v226, v226, v224
	v_mfma_f32_32x32x16_bf16 v[48:63], a[252:255], a[156:159], v[48:63]
	s_add_i32 s19, s29, 0x8c00
	s_mov_b32 s42, s19
	v_add_f32_e32 v231, v231, v227
	v_add_f32_e32 v226, v226, v228
	v_mfma_f32_32x32x16_bf16 v[32:47], a[252:255], a[188:191], v[32:47]
	s_add_i32 s43, s63, 0x880
	v_add_f32_e32 v231, v231, v229
	v_add_f32_e32 v226, v226, v230
	v_add_f32_e32 v216, v216, v225
	s_waitcnt vmcnt(0) lgkmcnt(0)
	s_barrier
	s_mov_b32 m0, s27
	v_mfma_f32_32x32x16_bf16 a[0:15], v[160:163], v[152:155], 0
	v_mov_b32_e32 v225, v216
	buffer_load_dwordx4 v222, s[12:15], s30 offen lds
	s_mov_b32 m0, s31
	v_mfma_f32_32x32x16_bf16 a[16:31], v[160:163], v[180:183], 0
	v_permlane32_swap_b32_e32 v216, v225
	v_add_f32_e32 v216, v216, v225
	buffer_load_dwordx4 v223, s[12:15], s33 offen lds
	ds_read_b128 a[192:195], v218 offset:0
	s_mov_b32 m0, s34
	v_mfma_f32_32x32x16_bf16 a[32:47], v[172:175], v[152:155], 0
	v_add_f32_e32 v225, v193, v216
	v_add_f32_e32 v216, v231, v226
	v_mov_b32_e32 v226, v216
	buffer_load_dwordx4 v222, s[12:15], s35 offen lds
	ds_read_b128 a[196:199], v219 offset:0
	s_mov_b32 m0, s36
	v_mfma_f32_32x32x16_bf16 a[48:63], v[172:175], v[180:183], 0
	v_permlane32_swap_b32_e32 v216, v226
	v_add_f32_e32 v216, v216, v226
	buffer_load_dwordx4 v223, s[12:15], s37 offen lds
	ds_read_b128 a[200:203], v220 offset:0
	s_mov_b32 m0, s38
	v_mfma_f32_32x32x16_bf16 a[64:79], v[168:171], v[152:155], 0
	v_add_f32_e32 v226, v193, v216
	buffer_load_dwordx4 v196, s[4:7], s0 offen lds
	ds_read_b128 a[204:207], v221 offset:0
	s_mov_b32 m0, s39
	v_mfma_f32_32x32x16_bf16 a[80:95], v[168:171], v[180:183], 0
	buffer_load_dwordx4 v196, s[4:7], s40 offen lds
	ds_read_b128 a[208:211], v218 offset:128
	s_mov_b32 m0, s41
	v_mfma_f32_32x32x16_bf16 a[96:111], v[176:179], v[152:155], 0
	buffer_load_dwordx4 v196, s[4:7], s1 offen lds
	ds_read_b128 a[212:215], v219 offset:128
	s_mov_b32 m0, s42
	v_mfma_f32_32x32x16_bf16 a[112:127], v[176:179], v[180:183], 0
	buffer_load_dwordx4 v196, s[4:7], s43 offen lds
	ds_read_b128 a[216:219], v220 offset:128
	v_mfma_f32_32x32x16_bf16 a[0:15], v[164:167], v[128:131], a[0:15]
	ds_read_b128 a[220:223], v221 offset:128
	v_cvt_pk_bf16_f32 v248, v248, v249
	v_cvt_pk_bf16_f32 v249, v250, v251
	v_cvt_pk_bf16_f32 v250, v252, v253
	v_cvt_pk_bf16_f32 v251, v254, v255
	v_lshrrev_b32_e32 v252, 1, v208
	buffer_store_dwordx4 v[248:251], v252, s[12:15], s56 offen sc1
	v_mbcnt_lo_u32_b32 v253, -1, 0
	v_mbcnt_hi_u32_b32 v253, -1, v253
	v_lshlrev_b32_e32 v253, 4, v253
	v_add_u32_e32 v253, s84, v253
	ds_read_b128 v[248:251], v253
	ds_read_b128 v[252:255], v253 offset:1024
	v_max3_f32 v152, v80, v81, v48
	v_max3_f32 v153, v82, v83, v49
	v_max3_f32 v152, v152, v50, v51
	v_mfma_f32_32x32x16_bf16 a[16:31], v[164:167], v[144:147], a[16:31]
	ds_read_b128 a[224:227], v218 offset:8192
	v_max3_f32 v152, v152, v84, v85
	v_max3_f32 v153, v153, v86, v87
	v_max3_f32 v152, v152, v52, v53
	v_max3_f32 v153, v153, v54, v55
	v_mfma_f32_32x32x16_bf16 a[32:47], v[156:159], v[128:131], a[32:47]
	ds_read_b128 a[228:231], v219 offset:8192
	v_max3_f32 v152, v152, v88, v89
	v_max3_f32 v153, v153, v90, v91
	v_max3_f32 v152, v152, v56, v57
	v_max3_f32 v153, v153, v58, v59
	v_mfma_f32_32x32x16_bf16 a[48:63], v[156:159], v[144:147], a[48:63]
	ds_read_b128 a[232:235], v220 offset:8192
	v_max3_f32 v152, v152, v92, v93
	v_max3_f32 v153, v153, v94, v95
	v_max3_f32 v152, v152, v60, v61
	v_max3_f32 v153, v153, v62, v63
	v_mfma_f32_32x32x16_bf16 a[64:79], v[148:151], v[128:131], a[64:79]
	ds_read_b128 a[236:239], v221 offset:8192
	v_max3_f32 v154, v64, v65, v32
	v_max3_f32 v155, v66, v67, v33
	v_max3_f32 v154, v154, v34, v35
	v_mfma_f32_32x32x16_bf16 a[80:95], v[148:151], v[144:147], a[80:95]
	ds_read_b128 a[240:243], v218 offset:8320
	v_max3_f32 v148, v154, v68, v69
	v_max3_f32 v149, v155, v70, v71
	v_max3_f32 v148, v148, v36, v37
	v_max3_f32 v149, v149, v38, v39
	v_mfma_f32_32x32x16_bf16 a[96:111], v[136:139], v[128:131], a[96:111]
	ds_read_b128 a[244:247], v219 offset:8320
	v_max3_f32 v128, v148, v72, v73
	v_max3_f32 v129, v149, v74, v75
	v_max3_f32 v128, v128, v40, v41
	v_max3_f32 v129, v129, v42, v43
	v_mfma_f32_32x32x16_bf16 a[112:127], v[136:139], v[144:147], a[112:127]
	ds_read_b128 a[248:251], v220 offset:8320
	v_max3_f32 v128, v128, v76, v77
	v_max3_f32 v129, v129, v78, v79
	v_max3_f32 v128, v128, v44, v45
	v_max3_f32 v130, v129, v46, v47
	v_mfma_f32_32x32x16_bf16 a[0:15], v[132:135], v[112:115], a[0:15]
	ds_read_b128 a[252:255], v221 offset:8320
	s_waitcnt lgkmcnt(8)
	v_pk_add_f32 v[200:201], v[248:249], v[200:201]
	v_pk_add_f32 v[202:203], v[250:251], v[202:203]
	v_pk_add_f32 v[204:205], v[252:253], v[204:205]
	v_pk_add_f32 v[206:207], v[254:255], v[206:207]
	v_cvt_pk_bf16_f32 v248, v248, v249
	v_cvt_pk_bf16_f32 v249, v250, v251
	v_cvt_pk_bf16_f32 v250, v252, v253
	v_cvt_pk_bf16_f32 v251, v254, v255
	v_lshrrev_b32_e32 v252, 1, v208
	buffer_store_dwordx4 v[248:251], v252, s[4:7], s56 offen sc1
	s_add_i32 s56, s56, 0x1000
	s_nop 1
	global_load_dwordx4 v[248:251], v208, s[54:55] nt
	global_load_dwordx4 v[252:255], v208, s[54:55] offset:16 nt
	s_add_u32 s54, s54, 0x2000
	s_addc_u32 s55, s55, 0
	s_mov_b32 m0, s84
	s_nop 0
	buffer_load_dwordx4 v208, s[80:83], s86 offen lds
	s_mov_b32 m0, s85
	s_nop 0
	buffer_load_dwordx4 v208, s[80:83], s86 offen offset:16 lds
	s_add_i32 s86, s86, 0x2000
	v_max_f32_e32 v129, v152, v153
	v_mov_b32_e32 v131, v129
	s_nop 1
	v_permlane32_swap_b32_e32 v129, v131
	v_max_f32_e32 v129, v129, v131
	v_mfma_f32_32x32x16_bf16 a[16:31], v[132:135], v[140:143], a[16:31]
	v_max_f32_e32 v128, v128, v130
	v_mov_b32_e32 v130, v128
	s_nop 1
	v_permlane32_swap_b32_e32 v128, v130
	v_max_f32_e32 v128, v128, v130
	v_max_f32_e32 v130, v129, v129
	v_max_f32_e32 v131, v128, v128
	v_max_f32_e32 v130, v130, v131
	s_mov_b32 s0, 0x41000000
	v_mfma_f32_32x32x16_bf16 a[32:47], v[124:127], v[112:115], a[32:47]
	v_cmp_lt_f32_e32 vcc, s0, v130
	s_cmp_lg_u64 vcc, 0
	s_cselect_b64 s[0:1], -1, 0
	s_cbranch_vccnz .LBB0_41
	v_mov_b32_e32 v216, 1.0

.LBB0_26:
	s_and_b64 vcc, exec, s[78:79]
	s_cbranch_vccnz .LBB0_11
.LBB0_27:
	global_load_dword v2, v41, s[64:65] sc1
	s_waitcnt vmcnt(0)
	s_mov_b64 s[78:79], -1
	v_cmp_eq_u32_e32 vcc, s70, v2
	s_cmp_eq_u64 vcc, exec
	s_cbranch_scc1 .LBB0_26
	s_sleep 8
	global_load_dword v2, v41, s[64:65] sc1
	s_waitcnt vmcnt(0)
	s_nop 0
	v_cmp_eq_u32_e32 vcc, s70, v2
	s_cmp_lg_u64 vcc, exec
	s_cbranch_scc0 .LBB0_26
	s_sleep 8
	global_load_dword v2, v41, s[64:65] sc1
	s_waitcnt vmcnt(0)
	s_nop 0
	v_cmp_eq_u32_e32 vcc, s70, v2
	s_cmp_lg_u64 vcc, exec
	s_cbranch_scc0 .LBB0_26
	s_sleep 8
	global_load_dword v2, v41, s[64:65] sc1
	s_waitcnt vmcnt(0)
	s_nop 0
	v_cmp_eq_u32_e32 vcc, s70, v2
	s_cmp_lg_u64 vcc, exec
	s_cbranch_scc0 .LBB0_26
	s_sleep 8
	global_load_dword v2, v41, s[64:65] sc1
	s_waitcnt vmcnt(0)
	s_nop 0
	v_cmp_eq_u32_e32 vcc, s70, v2
	s_cmp_lg_u64 vcc, exec
	s_cbranch_scc0 .LBB0_26
	s_sleep 8
	global_load_dword v2, v41, s[64:65] sc1
	s_waitcnt vmcnt(0)
	s_nop 0
	v_cmp_eq_u32_e32 vcc, s70, v2
	s_cmp_lg_u64 vcc, exec
	s_cbranch_scc0 .LBB0_26
	s_sleep 8
	global_load_dword v2, v41, s[64:65] sc1
	s_waitcnt vmcnt(0)
	s_nop 0
	v_cmp_eq_u32_e32 vcc, s70, v2
	s_cmp_lg_u64 vcc, exec
	s_cbranch_scc0 .LBB0_26
	s_sleep 8
	global_load_dword v2, v41, s[64:65] sc1
	s_waitcnt vmcnt(0)
	s_nop 0
	v_cmp_eq_u32_e32 vcc, s70, v2
	s_cmp_lg_u64 vcc, exec
	s_cbranch_scc0 .LBB0_26
	s_add_i32 s53, s53, -8
	s_cmp_eq_u32 s53, 0
	s_cselect_b64 s[78:79], -1, 0
	s_sleep 8
	s_branch .LBB0_26
